# stack3: v131 + epidrain1 (unit-loop-head store-drain waits of the down-proj / layer-1 QKV GEMMs skipped on the back edge)
# baseline (speedup 1.0000x reference)
.LBB0_787:
	s_add_u32 s38, s4, 0x4b400000
	s_addc_u32 s39, s5, 0
	v_lshrrev_b32_e32 v3, 1, v194
	s_add_u32 s4, s18, 0x80
	v_and_b32_e32 v3, 24, v3
	s_addc_u32 s5, s19, 0
	v_and_b32_e32 v2, 15, v194
	v_lshlrev_b32_e32 v4, 1, v3
	s_cmp_lg_u64 s[16:17], 0
	v_lshl_or_b32 v197, s43, 6, v2
	v_lshl_or_b32 v2, v2, 6, v4
	v_lshlrev_b32_e32 v4, 2, v194
	s_cselect_b64 s[40:41], -1, 0
	s_lshl_b32 s43, s43, 13
	v_and_b32_e32 v4, 32, v4
	v_bitop3_b32 v5, v2, s43, v4 bitop3:0xde
	s_lshl_b32 s43, s47, 5
	s_and_b32 s47, s43, 0x60
	s_lshl_b32 s43, s47, 7
	s_add_u32 s48, s20, 0x80
	v_bitop3_b32 v2, v2, s43, v4 bitop3:0xde
	s_waitcnt vmcnt(2)
	s_barrier
	s_addc_u32 s49, s21, 0
	s_add_i32 s77, s73, 0x18000
	s_mov_b32 s43, m0
	s_mov_b32 m0, s77
	s_nop 0
	global_load_lds_dwordx4 v195, s[48:49]
	s_mov_b32 m0, s43
	s_add_i32 s78, s73, 0x1a000
	s_mov_b32 s43, m0
	s_mov_b32 m0, s78
	s_nop 0
	global_load_lds_dwordx4 v196, s[48:49]
	s_mov_b32 m0, s43
	s_add_i32 s79, s73, 0x8000
	s_mov_b32 s43, m0
	s_mov_b32 m0, s79
	s_nop 0
	global_load_lds_dwordx4 v216, s[4:5]
	s_mov_b32 m0, s43
	s_add_i32 s80, s73, 0xa000
	s_mov_b32 s43, m0
	s_mov_b32 m0, s80
	s_nop 0
	global_load_lds_dwordx4 v218, s[4:5]
	s_mov_b32 m0, s43
	s_add_u32 s4, s20, 0x20080
	s_addc_u32 s5, s21, 0
	s_add_i32 s81, s73, 0x1c000
	s_mov_b32 s43, m0
	s_mov_b32 m0, s81
	s_nop 0
	global_load_lds_dwordx4 v195, s[4:5]
	s_mov_b32 m0, s43
	s_add_i32 s82, s73, 0x1e000
	s_mov_b32 s43, m0
	s_mov_b32 m0, s82
	s_nop 0
	global_load_lds_dwordx4 v196, s[4:5]
	s_mov_b32 m0, s43
	s_waitcnt vmcnt(6)
	s_add_i32 s4, s73, 0xc000
	s_cmpk_lt_u32 s42, 0x100
	v_add_u32_e32 v199, 0, v2
	s_cselect_b64 s[42:43], -1, 0
	v_or_b32_e32 v198, s47, v3
	v_add_u32_e32 v200, 0x10000, v199
	v_add_u32_e32 v201, 0x14000, v199
	v_add_u32_e32 v202, 0, v5
	v_mov_b32_e32 v203, s4
	v_mov_b32_e32 v204, s73
	v_mov_b32_e32 v205, s13
	v_mov_b32_e32 v206, s15
	v_mov_b32_e32 v207, s44
	v_mov_b32_e32 v209, s46
	s_mov_b32 s44, 0x3d000000
	s_mov_b32 s83, 0x40000
	s_mov_b64 s[46:47], 0x48000
	s_mov_b32 s84, 0x48000
	s_mov_b64 s[48:49], 0x50000
	s_mov_b32 s85, 0x50000
	s_mov_b64 s[50:51], 0x58000
	s_mov_b32 s86, 0x58000
	v_mov_b32_e32 v210, 1
	s_barrier
	v_and_b32_e32 v250, 63, v0
	v_and_b32_e32 v251, 15, v250
	v_lshrrev_b32_e32 v252, 4, v250
	v_readfirstlane_b32 s99, v0
	s_lshr_b32 s99, s99, 6
	s_and_b32 s100, s99, 3
	s_lshr_b32 s101, s99, 2
	s_lshl_b32 s100, s100, 2
	v_add_u32_e32 v253, s100, v252
	v_xor_b32_e32 v254, v253, v251
	s_lshl_b32 s101, s101, 12
	s_add_i32 s101, s101, 0xc000
	v_lshlrev_b32_e32 v240, 8, v251
	v_lshl_add_u32 v240, v254, 4, v240
	v_add_u32_e32 v240, s101, v240
	v_lshlrev_b32_e32 v241, 8, v253
	v_lshl_add_u32 v241, v254, 4, v241
	v_add_u32_e32 v241, s101, v241
	v_sub_u32_e32 v242, v253, v251
	v_lshlrev_b32_e32 v242, 11, v242
	v_lshl_add_u32 v242, v251, 4, v242
	v_lshlrev_b32_e32 v244, 4, v253
	v_sub_u32_e32 v242, v242, v244
	v_ashrrev_i32_e32 v243, 31, v242
	s_mov_b32 s98, 0
	s_branch .LBB0_790

.LBB0_789:
	s_mov_b32 s98, 1
	s_andn2_b64 vcc, exec, s[4:5]
	v_mov_b32_e32 v217, v214
	v_mov_b32_e32 v215, v213
	v_mov_b32_e32 v218, v212
	v_mov_b32_e32 v216, v211
	s_cbranch_vccz .LBB0_826
.LBB0_790:
	s_mov_b32 s56, s14
	s_mov_b32 s14, s69
	s_ashr_i32 s15, s69, 31
	s_mov_b64 s[4:5], s[20:21]
	s_lshl_b64 s[20:21], s[14:15], 20
	s_add_u32 s15, s70, s20
	s_mov_b64 s[54:55], s[58:59]
	s_mov_b32 s57, s12
	s_mov_b32 s12, s67
	s_addc_u32 s58, s71, s21
	s_ashr_i32 s13, s67, 31
	s_lshl_b64 s[20:21], s[12:13], 18
	s_add_u32 s20, s15, s20
	s_addc_u32 s21, s58, s21
	s_and_b64 s[58:59], s[54:55], exec
	s_cselect_b32 s13, s21, s5
	s_cselect_b32 s15, s20, s4
	s_add_u32 s89, s4, 0x100
	v_mov_b32_e32 v66, 0
	s_mov_b32 s87, s45
	s_mov_b32 s45, s68
	v_mov_b32_e32 v211, v23
	v_mov_b32_e32 v212, v25
	v_mov_b32_e32 v213, v22
	v_mov_b32_e32 v214, v24
	s_addc_u32 s90, s5, 0
	s_mov_b32 s91, -2
	s_mov_b64 s[58:59], 0
	v_mov_b32_e32 v67, v66
	v_mov_b32_e32 v68, v66
	v_mov_b32_e32 v69, v66
	v_mov_b32_e32 v70, v66
	v_mov_b32_e32 v71, v66
	v_mov_b32_e32 v72, v66
	v_mov_b32_e32 v73, v66
	v_mov_b32_e32 v78, v66
	v_mov_b32_e32 v79, v66
	v_mov_b32_e32 v80, v66
	v_mov_b32_e32 v81, v66
	v_mov_b32_e32 v86, v66
	v_mov_b32_e32 v87, v66
	v_mov_b32_e32 v88, v66
	v_mov_b32_e32 v89, v66
	v_mov_b32_e32 v94, v66
	v_mov_b32_e32 v95, v66
	v_mov_b32_e32 v96, v66
	v_mov_b32_e32 v97, v66
	v_mov_b32_e32 v102, v66
	v_mov_b32_e32 v103, v66
	v_mov_b32_e32 v104, v66
	v_mov_b32_e32 v105, v66
	v_mov_b32_e32 v110, v66
	v_mov_b32_e32 v111, v66
	v_mov_b32_e32 v112, v66
	v_mov_b32_e32 v113, v66
	v_mov_b32_e32 v118, v66
	v_mov_b32_e32 v119, v66
	v_mov_b32_e32 v120, v66
	v_mov_b32_e32 v121, v66
	v_mov_b32_e32 v74, v66
	v_mov_b32_e32 v75, v66
	v_mov_b32_e32 v76, v66
	v_mov_b32_e32 v77, v66
	v_mov_b32_e32 v82, v66
	v_mov_b32_e32 v83, v66
	v_mov_b32_e32 v84, v66
	v_mov_b32_e32 v85, v66
	v_mov_b32_e32 v90, v66
	v_mov_b32_e32 v91, v66
	v_mov_b32_e32 v92, v66
	v_mov_b32_e32 v93, v66
	v_mov_b32_e32 v98, v66
	v_mov_b32_e32 v99, v66
	v_mov_b32_e32 v100, v66
	v_mov_b32_e32 v101, v66
	v_mov_b32_e32 v106, v66
	v_mov_b32_e32 v107, v66
	v_mov_b32_e32 v108, v66
	v_mov_b32_e32 v109, v66
	v_mov_b32_e32 v114, v66
	v_mov_b32_e32 v115, v66
	v_mov_b32_e32 v116, v66
	v_mov_b32_e32 v117, v66
	v_mov_b32_e32 v122, v66
	v_mov_b32_e32 v123, v66
	v_mov_b32_e32 v124, v66
	v_mov_b32_e32 v125, v66
	v_mov_b32_e32 v126, v66
	v_mov_b32_e32 v127, v66
	v_mov_b32_e32 v128, v66
	v_mov_b32_e32 v129, v66
	s_cmp_lg_u32 s98, 0
	s_cbranch_scc1 .Led_0
	s_waitcnt vmcnt(6)
.Led_0:
	v_mov_b32_e32 v130, v66
	v_mov_b32_e32 v131, v66
	v_mov_b32_e32 v132, v66
	v_mov_b32_e32 v133, v66
	v_mov_b32_e32 v134, v66
	v_mov_b32_e32 v135, v66
	v_mov_b32_e32 v136, v66
	v_mov_b32_e32 v137, v66
	s_cmp_lg_u32 s98, 0
	s_cbranch_scc1 .Led_1
	s_waitcnt vmcnt(5)
.Led_1:
	v_mov_b32_e32 v142, v66
	v_mov_b32_e32 v143, v66
	v_mov_b32_e32 v144, v66
	v_mov_b32_e32 v145, v66
	s_cmp_lg_u32 s98, 0
	s_cbranch_scc1 .Led_2
	s_waitcnt vmcnt(3)
.Led_2:
	v_mov_b32_e32 v150, v66
	v_mov_b32_e32 v151, v66
	v_mov_b32_e32 v152, v66
	v_mov_b32_e32 v153, v66
	s_cmp_lg_u32 s98, 0
	s_cbranch_scc1 .Led_3
	s_waitcnt vmcnt(1)
.Led_3:
	v_mov_b32_e32 v158, v66
	v_mov_b32_e32 v159, v66
	v_mov_b32_e32 v160, v66
	v_mov_b32_e32 v161, v66
	v_mov_b32_e32 v166, v66
	v_mov_b32_e32 v167, v66
	v_mov_b32_e32 v168, v66
	v_mov_b32_e32 v169, v66
	v_mov_b32_e32 v174, v66
	v_mov_b32_e32 v175, v66
	v_mov_b32_e32 v176, v66
	v_mov_b32_e32 v177, v66
	v_mov_b32_e32 v182, v66
	v_mov_b32_e32 v183, v66
	v_mov_b32_e32 v184, v66
	v_mov_b32_e32 v185, v66
	v_mov_b32_e32 v138, v66
	v_mov_b32_e32 v139, v66
	v_mov_b32_e32 v140, v66
	v_mov_b32_e32 v141, v66
	v_mov_b32_e32 v146, v66
	v_mov_b32_e32 v147, v66
	v_mov_b32_e32 v148, v66
	v_mov_b32_e32 v149, v66
	s_cmp_lg_u32 s98, 0
	s_cbranch_scc1 .Led_4
	s_waitcnt vmcnt(0)
.Led_4:
	v_mov_b32_e32 v154, v66
	v_mov_b32_e32 v155, v66
	v_mov_b32_e32 v156, v66
	v_mov_b32_e32 v157, v66
	v_mov_b32_e32 v162, v66
	v_mov_b32_e32 v163, v66
	v_mov_b32_e32 v164, v66
	v_mov_b32_e32 v165, v66
	v_mov_b32_e32 v170, v66
	v_mov_b32_e32 v171, v66
	v_mov_b32_e32 v172, v66
	v_mov_b32_e32 v173, v66
	v_mov_b32_e32 v178, v66
	v_mov_b32_e32 v179, v66
	v_mov_b32_e32 v180, v66
	v_mov_b32_e32 v181, v66
	v_mov_b32_e32 v186, v66
	v_mov_b32_e32 v187, v66
	v_mov_b32_e32 v188, v66
	v_mov_b32_e32 v189, v66
	v_mov_b32_e32 v190, v66
	v_mov_b32_e32 v191, v66
	v_mov_b32_e32 v192, v66
	v_mov_b32_e32 v193, v66
	s_branch .LBB0_792

.LBB0_949:
	s_add_u32 s55, s4, 0x25b00000
	s_addc_u32 s56, s5, 0
	v_lshrrev_b32_e32 v3, 1, v1
	s_add_u32 s18, s4, 0x200000
	v_and_b32_e32 v3, 24, v3
	s_addc_u32 s19, s5, 0
	v_and_b32_e32 v2, 15, v1
	v_lshlrev_b32_e32 v4, 1, v3
	s_add_u32 s4, s12, 0x80
	v_lshl_or_b32 v200, s6, 6, v2
	v_lshl_or_b32 v2, v2, 6, v4
	v_lshlrev_b32_e32 v4, 2, v1
	s_addc_u32 s5, s13, 0
	s_lshl_b32 s6, s6, 13
	v_and_b32_e32 v4, 32, v4
	v_bitop3_b32 v5, v2, s6, v4 bitop3:0xde
	s_lshl_b32 s6, s21, 5
	s_and_b32 s6, s6, 0x60
	s_lshl_b32 s21, s6, 7
	s_add_u32 s42, s14, 0x80
	v_bitop3_b32 v2, v2, s21, v4 bitop3:0xde
	s_waitcnt vmcnt(2)
	s_barrier
	s_addc_u32 s43, s15, 0
	s_add_i32 s57, s50, 0x18000
	s_mov_b32 s21, m0
	s_mov_b32 m0, s57
	s_nop 0
	global_load_lds_dwordx4 v198, s[42:43]
	s_mov_b32 m0, s21
	s_add_i32 s58, s50, 0x1a000
	s_mov_b32 s21, m0
	s_mov_b32 m0, s58
	s_nop 0
	global_load_lds_dwordx4 v199, s[42:43]
	s_mov_b32 m0, s21
	s_add_i32 s59, s50, 0x8000
	s_mov_b32 s21, m0
	s_mov_b32 m0, s59
	s_nop 0
	global_load_lds_dwordx4 v221, s[4:5]
	s_mov_b32 m0, s21
	s_add_i32 s60, s50, 0xa000
	s_mov_b32 s21, m0
	s_mov_b32 m0, s60
	s_nop 0
	global_load_lds_dwordx4 v223, s[4:5]
	s_mov_b32 m0, s21
	s_add_u32 s4, s14, 0x20080
	s_addc_u32 s5, s15, 0
	s_add_i32 s61, s50, 0x1c000
	s_mov_b32 s21, m0
	s_mov_b32 m0, s61
	s_nop 0
	global_load_lds_dwordx4 v198, s[4:5]
	s_mov_b32 m0, s21
	s_add_i32 s62, s50, 0x1e000
	s_mov_b32 s21, m0
	s_mov_b32 m0, s62
	s_nop 0
	global_load_lds_dwordx4 v199, s[4:5]
	s_mov_b32 m0, s21
	s_waitcnt vmcnt(6)
	s_add_i32 s4, s50, 0xc000
	s_cmpk_lt_u32 s20, 0x100
	v_add_u32_e32 v202, 0, v2
	s_cselect_b64 s[20:21], -1, 0
	v_or_b32_e32 v201, s6, v3
	v_add_u32_e32 v203, 0x10000, v202
	v_add_u32_e32 v204, 0x14000, v202
	v_add_u32_e32 v205, 0, v5
	v_mov_b32_e32 v206, s4
	v_mov_b32_e32 v207, s50
	v_mov_b32_e32 v209, s7
	v_mov_b32_e32 v210, s11
	v_mov_b32_e32 v211, s28
	v_mov_b32_e32 v212, s38
	s_movk_i32 s63, 0xc4
	s_mov_b32 s64, 0x7f9e0
	v_mov_b32_e32 v195, 0
	s_mov_b32 s28, 0x3d000000
	s_mov_b32 s65, 0x7fbe0
	s_mov_b32 s66, 0x7fde0
	s_mov_b32 s67, 0x7ffe0
	v_mov_b64_e32 v[196:197], 0x617
	v_mov_b32_e32 v213, 1
	v_mov_b32_e32 v214, 0x3e38aa3b
	v_mov_b32_e32 v215, 0x3eb504f3
	v_mov_b32_e32 v216, 0x3f0293ee
	s_barrier
	s_mov_b32 s98, 0
	s_branch .LBB0_952

.LBB0_951:
	s_mov_b32 s98, 1
	s_andn2_b64 vcc, exec, s[4:5]
	v_mov_b32_e32 v222, v220
	v_mov_b32_e32 v194, v219
	v_mov_b32_e32 v223, v218
	v_mov_b32_e32 v221, v217
	s_cbranch_vccz .LBB0_1072
.LBB0_952:
	s_mov_b32 s46, s10
	s_mov_b32 s10, s27
	s_ashr_i32 s11, s27, 31
	s_lshl_b64 s[6:7], s[10:11], 18
	s_mov_b64 s[4:5], s[14:15]
	s_add_u32 s14, s35, s6
	s_addc_u32 s15, s48, s7
	s_and_b64 s[6:7], s[40:41], exec
	s_cselect_b32 s11, s15, s5
	s_cselect_b32 s68, s14, s4
	s_add_u32 s69, s4, 0x100
	s_mov_b64 s[38:39], s[40:41]
	s_mov_b32 s47, s3
	s_mov_b32 s3, s29
	v_mov_b32_e32 v217, v27
	v_mov_b32_e32 v218, v29
	v_mov_b32_e32 v219, v26
	v_mov_b32_e32 v220, v28
	s_addc_u32 s70, s5, 0
	s_mov_b32 s71, -2
	s_mov_b64 s[6:7], 0
	v_mov_b32_e32 v66, 0
	v_mov_b32_e32 v67, v195
	v_mov_b32_e32 v68, v195
	v_mov_b32_e32 v69, v195
	v_mov_b32_e32 v70, 0
	v_mov_b32_e32 v71, v195
	v_mov_b32_e32 v72, v195
	v_mov_b32_e32 v73, v195
	v_mov_b32_e32 v82, 0
	v_mov_b32_e32 v83, v195
	v_mov_b32_e32 v84, v195
	v_mov_b32_e32 v85, v195
	v_mov_b32_e32 v86, 0
	v_mov_b32_e32 v87, v195
	v_mov_b32_e32 v88, v195
	v_mov_b32_e32 v89, v195
	v_mov_b32_e32 v98, 0
	v_mov_b32_e32 v99, v195
	v_mov_b32_e32 v100, v195
	v_mov_b32_e32 v101, v195
	v_mov_b32_e32 v102, 0
	v_mov_b32_e32 v103, v195
	v_mov_b32_e32 v104, v195
	v_mov_b32_e32 v105, v195
	v_mov_b32_e32 v114, 0
	v_mov_b32_e32 v115, v195
	v_mov_b32_e32 v116, v195
	v_mov_b32_e32 v117, v195
	v_mov_b32_e32 v118, 0
	v_mov_b32_e32 v119, v195
	v_mov_b32_e32 v120, v195
	v_mov_b32_e32 v121, v195
	v_mov_b32_e32 v74, 0
	v_mov_b32_e32 v75, v195
	v_mov_b32_e32 v76, v195
	v_mov_b32_e32 v77, v195
	v_mov_b32_e32 v78, 0
	v_mov_b32_e32 v79, v195
	v_mov_b32_e32 v80, v195
	v_mov_b32_e32 v81, v195
	v_mov_b32_e32 v90, 0
	v_mov_b32_e32 v91, v195
	v_mov_b32_e32 v92, v195
	v_mov_b32_e32 v93, v195
	v_mov_b32_e32 v94, 0
	v_mov_b32_e32 v95, v195
	v_mov_b32_e32 v96, v195
	v_mov_b32_e32 v97, v195
	v_mov_b32_e32 v106, 0
	v_mov_b32_e32 v107, v195
	v_mov_b32_e32 v108, v195
	v_mov_b32_e32 v109, v195
	v_mov_b32_e32 v110, 0
	v_mov_b32_e32 v111, v195
	v_mov_b32_e32 v112, v195
	v_mov_b32_e32 v113, v195
	v_mov_b32_e32 v122, 0
	v_mov_b32_e32 v123, v195
	v_mov_b32_e32 v124, v195
	v_mov_b32_e32 v125, v195
	v_mov_b32_e32 v126, 0
	v_mov_b32_e32 v127, v195
	v_mov_b32_e32 v128, v195
	v_mov_b32_e32 v129, v195
	s_cmp_lg_u32 s98, 0
	s_cbranch_scc1 .Led_5
	s_waitcnt vmcnt(6)
.Led_5:
	v_mov_b32_e32 v130, 0
	v_mov_b32_e32 v131, v195
	v_mov_b32_e32 v132, v195
	v_mov_b32_e32 v133, v195
	v_mov_b32_e32 v134, 0
	v_mov_b32_e32 v135, v195
	v_mov_b32_e32 v136, v195
	v_mov_b32_e32 v137, v195
	s_cmp_lg_u32 s98, 0
	s_cbranch_scc1 .Led_6
	s_waitcnt vmcnt(2)
.Led_6:
	v_mov_b32_e32 v146, 0
	v_mov_b32_e32 v147, v195
	v_mov_b32_e32 v148, v195
	v_mov_b32_e32 v149, v195
	v_mov_b32_e32 v150, 0
	v_mov_b32_e32 v151, v195
	v_mov_b32_e32 v152, v195
	v_mov_b32_e32 v153, v195
	v_mov_b32_e32 v162, 0
	v_mov_b32_e32 v163, v195
	v_mov_b32_e32 v164, v195
	v_mov_b32_e32 v165, v195
	v_mov_b32_e32 v166, 0
	v_mov_b32_e32 v167, v195
	v_mov_b32_e32 v168, v195
	v_mov_b32_e32 v169, v195
	v_mov_b32_e32 v178, 0
	v_mov_b32_e32 v179, v195
	v_mov_b32_e32 v180, v195
	v_mov_b32_e32 v181, v195
	v_mov_b32_e32 v182, 0
	v_mov_b32_e32 v183, v195
	v_mov_b32_e32 v184, v195
	v_mov_b32_e32 v185, v195
	v_mov_b32_e32 v138, 0
	v_mov_b32_e32 v139, v195
	v_mov_b32_e32 v140, v195
	v_mov_b32_e32 v141, v195
	v_mov_b32_e32 v142, 0
	v_mov_b32_e32 v143, v195
	v_mov_b32_e32 v144, v195
	v_mov_b32_e32 v145, v195
	s_cmp_lg_u32 s98, 0
	s_cbranch_scc1 .Led_7
	s_waitcnt vmcnt(0)
.Led_7:
	v_mov_b32_e32 v154, 0
	v_mov_b32_e32 v155, v195
	v_mov_b32_e32 v156, v195
	v_mov_b32_e32 v157, v195
	v_mov_b32_e32 v158, 0
	v_mov_b32_e32 v159, v195
	v_mov_b32_e32 v160, v195
	v_mov_b32_e32 v161, v195
	v_mov_b32_e32 v170, 0
	v_mov_b32_e32 v171, v195
	v_mov_b32_e32 v172, v195
	v_mov_b32_e32 v173, v195
	v_mov_b32_e32 v174, 0
	v_mov_b32_e32 v175, v195
	v_mov_b32_e32 v176, v195
	v_mov_b32_e32 v177, v195
	v_mov_b32_e32 v186, 0
	v_mov_b32_e32 v187, v195
	v_mov_b32_e32 v188, v195
	v_mov_b32_e32 v189, v195
	v_mov_b32_e32 v190, 0
	v_mov_b32_e32 v191, v195
	v_mov_b32_e32 v192, v195
	v_mov_b32_e32 v193, v195
	s_branch .LBB0_954

.LBB0_1863:
	s_add_u32 s28, s28, 0x4b400000
	s_addc_u32 s29, s29, 0
	v_lshrrev_b32_e32 v3, 1, v0
	s_add_u32 s72, s36, 0x20000
	v_and_b32_e32 v3, 24, v3
	s_addc_u32 s73, s37, 0
	v_and_b32_e32 v2, 15, v0
	v_lshlrev_b32_e32 v4, 1, v3
	s_add_u32 s36, s16, 0x80
	v_lshl_or_b32 v195, s38, 6, v2
	v_lshl_or_b32 v2, v2, 6, v4
	v_lshlrev_b32_e32 v4, 2, v0
	s_addc_u32 s37, s17, 0
	s_lshl_b32 s38, s38, 13
	v_and_b32_e32 v4, 32, v4
	v_bitop3_b32 v5, v2, s38, v4 bitop3:0xde
	s_lshl_b32 s38, s41, 5
	s_and_b32 s38, s38, 0x60
	s_lshl_b32 s41, s38, 7
	s_add_u32 s42, s18, 0x80
	v_bitop3_b32 v2, v2, s41, v4 bitop3:0xde
	s_waitcnt vmcnt(2)
	s_barrier
	s_addc_u32 s43, s19, 0
	s_add_i32 s74, s68, 0x18000
	s_mov_b32 s41, m0
	s_mov_b32 m0, s74
	s_nop 0
	global_load_lds_dwordx4 v1, s[42:43]
	s_mov_b32 m0, s41
	s_add_i32 s75, s68, 0x1a000
	s_mov_b32 s41, m0
	s_mov_b32 m0, s75
	s_nop 0
	global_load_lds_dwordx4 v194, s[42:43]
	s_mov_b32 m0, s41
	s_add_i32 s76, s68, 0x8000
	s_mov_b32 s41, m0
	s_mov_b32 m0, s76
	s_nop 0
	global_load_lds_dwordx4 v214, s[36:37]
	s_mov_b32 m0, s41
	s_add_i32 s77, s68, 0xa000
	s_mov_b32 s41, m0
	s_mov_b32 m0, s77
	s_nop 0
	global_load_lds_dwordx4 v216, s[36:37]
	s_mov_b32 m0, s41
	s_add_u32 s36, s18, 0x20080
	s_addc_u32 s37, s19, 0
	s_add_i32 s78, s68, 0x1c000
	s_mov_b32 s41, m0
	s_mov_b32 m0, s78
	s_nop 0
	global_load_lds_dwordx4 v1, s[36:37]
	s_mov_b32 m0, s41
	s_add_i32 s79, s68, 0x1e000
	s_mov_b32 s41, m0
	s_mov_b32 m0, s79
	s_nop 0
	global_load_lds_dwordx4 v194, s[36:37]
	s_mov_b32 m0, s41
	s_waitcnt vmcnt(6)
	s_add_i32 s41, s68, 0xc000
	s_cmpk_lt_u32 s30, 0x100
	v_add_u32_e32 v197, 0, v2
	s_cselect_b64 s[36:37], -1, 0
	v_or_b32_e32 v196, s38, v3
	v_add_u32_e32 v198, 0x10000, v197
	v_add_u32_e32 v199, 0x14000, v197
	v_add_u32_e32 v200, 0, v5
	v_mov_b32_e32 v201, s41
	v_mov_b32_e32 v202, s68
	v_mov_b32_e32 v203, s13
	v_mov_b32_e32 v204, s15
	v_mov_b32_e32 v205, s39
	v_mov_b32_e32 v206, s40
	s_mov_b32 s30, 0x3d000000
	s_mov_b64 s[38:39], 0x40000
	s_mov_b32 s80, 0x40000
	s_mov_b64 s[40:41], 0x48000
	s_mov_b32 s81, 0x48000
	s_mov_b64 s[42:43], 0x50000
	s_mov_b32 s82, 0x50000
	s_mov_b64 s[44:45], 0x58000
	s_mov_b32 s83, 0x58000
	v_mov_b32_e32 v207, 1
	s_barrier
	v_and_b32_e32 v250, 63, v0
	v_and_b32_e32 v251, 15, v250
	v_lshrrev_b32_e32 v252, 4, v250
	v_readfirstlane_b32 s99, v0
	s_lshr_b32 s99, s99, 6
	s_and_b32 s100, s99, 3
	s_lshr_b32 s101, s99, 2
	s_lshl_b32 s100, s100, 2
	v_add_u32_e32 v253, s100, v252
	v_xor_b32_e32 v254, v253, v251
	s_lshl_b32 s101, s101, 12
	s_add_i32 s101, s101, 0xc000
	v_lshlrev_b32_e32 v240, 8, v251
	v_lshl_add_u32 v240, v254, 4, v240
	v_add_u32_e32 v240, s101, v240
	v_lshlrev_b32_e32 v241, 8, v253
	v_lshl_add_u32 v241, v254, 4, v241
	v_add_u32_e32 v241, s101, v241
	v_sub_u32_e32 v242, v253, v251
	v_lshlrev_b32_e32 v242, 11, v242
	v_lshl_add_u32 v242, v251, 4, v242
	v_lshlrev_b32_e32 v244, 4, v253
	v_sub_u32_e32 v242, v242, v244
	v_ashrrev_i32_e32 v243, 31, v242
	s_mov_b32 s98, 0
	s_branch .LBB0_1866

.LBB0_1865:
	s_mov_b32 s98, 1
	s_andn2_b64 vcc, exec, s[46:47]
	v_mov_b32_e32 v215, v212
	v_mov_b32_e32 v213, v211
	v_mov_b32_e32 v216, v210
	v_mov_b32_e32 v214, v209
	s_cbranch_vccz .LBB0_1894
.LBB0_1866:
	s_mov_b32 s48, s14
	s_mov_b32 s14, s64
	s_ashr_i32 s15, s64, 31
	s_mov_b64 s[46:47], s[4:5]
	s_mov_b64 s[4:5], s[18:19]
	s_lshl_b64 s[18:19], s[14:15], 20
	s_add_u32 s15, s65, s18
	s_mov_b32 s49, s12
	s_mov_b32 s12, s62
	s_addc_u32 s50, s66, s19
	s_ashr_i32 s13, s62, 31
	s_lshl_b64 s[18:19], s[12:13], 18
	s_add_u32 s18, s15, s18
	s_addc_u32 s19, s50, s19
	s_and_b64 s[50:51], s[46:47], exec
	s_cselect_b32 s13, s19, s5
	s_cselect_b32 s15, s18, s4
	s_add_u32 s85, s4, 0x100
	v_mov_b32_e32 v66, 0
	s_mov_b32 s84, s53
	s_mov_b32 s53, s63
	v_mov_b32_e32 v209, v21
	v_mov_b32_e32 v210, v23
	v_mov_b32_e32 v211, v20
	v_mov_b32_e32 v212, v22
	s_addc_u32 s86, s5, 0
	s_mov_b32 s87, -2
	s_mov_b64 s[50:51], 0
	v_mov_b32_e32 v67, v66
	v_mov_b32_e32 v68, v66
	v_mov_b32_e32 v69, v66
	v_mov_b32_e32 v70, v66
	v_mov_b32_e32 v71, v66
	v_mov_b32_e32 v72, v66
	v_mov_b32_e32 v73, v66
	v_mov_b32_e32 v78, v66
	v_mov_b32_e32 v79, v66
	v_mov_b32_e32 v80, v66
	v_mov_b32_e32 v81, v66
	v_mov_b32_e32 v86, v66
	v_mov_b32_e32 v87, v66
	v_mov_b32_e32 v88, v66
	v_mov_b32_e32 v89, v66
	v_mov_b32_e32 v94, v66
	v_mov_b32_e32 v95, v66
	v_mov_b32_e32 v96, v66
	v_mov_b32_e32 v97, v66
	v_mov_b32_e32 v102, v66
	v_mov_b32_e32 v103, v66
	v_mov_b32_e32 v104, v66
	v_mov_b32_e32 v105, v66
	v_mov_b32_e32 v110, v66
	v_mov_b32_e32 v111, v66
	v_mov_b32_e32 v112, v66
	v_mov_b32_e32 v113, v66
	v_mov_b32_e32 v118, v66
	v_mov_b32_e32 v119, v66
	v_mov_b32_e32 v120, v66
	v_mov_b32_e32 v121, v66
	v_mov_b32_e32 v74, v66
	v_mov_b32_e32 v75, v66
	v_mov_b32_e32 v76, v66
	v_mov_b32_e32 v77, v66
	v_mov_b32_e32 v82, v66
	v_mov_b32_e32 v83, v66
	v_mov_b32_e32 v84, v66
	v_mov_b32_e32 v85, v66
	v_mov_b32_e32 v90, v66
	v_mov_b32_e32 v91, v66
	v_mov_b32_e32 v92, v66
	v_mov_b32_e32 v93, v66
	v_mov_b32_e32 v98, v66
	v_mov_b32_e32 v99, v66
	v_mov_b32_e32 v100, v66
	v_mov_b32_e32 v101, v66
	v_mov_b32_e32 v106, v66
	v_mov_b32_e32 v107, v66
	v_mov_b32_e32 v108, v66
	v_mov_b32_e32 v109, v66
	v_mov_b32_e32 v114, v66
	v_mov_b32_e32 v115, v66
	v_mov_b32_e32 v116, v66
	v_mov_b32_e32 v117, v66
	v_mov_b32_e32 v122, v66
	v_mov_b32_e32 v123, v66
	v_mov_b32_e32 v124, v66
	v_mov_b32_e32 v125, v66
	v_mov_b32_e32 v126, v66
	v_mov_b32_e32 v127, v66
	v_mov_b32_e32 v128, v66
	v_mov_b32_e32 v129, v66
	v_mov_b32_e32 v130, v66
	v_mov_b32_e32 v131, v66
	v_mov_b32_e32 v132, v66
	v_mov_b32_e32 v133, v66
	v_mov_b32_e32 v134, v66
	v_mov_b32_e32 v135, v66
	v_mov_b32_e32 v136, v66
	v_mov_b32_e32 v137, v66
	v_mov_b32_e32 v138, v66
	v_mov_b32_e32 v139, v66
	v_mov_b32_e32 v140, v66
	v_mov_b32_e32 v141, v66
	v_mov_b32_e32 v142, v66
	v_mov_b32_e32 v143, v66
	v_mov_b32_e32 v144, v66
	v_mov_b32_e32 v145, v66
	v_mov_b32_e32 v146, v66
	v_mov_b32_e32 v147, v66
	v_mov_b32_e32 v148, v66
	v_mov_b32_e32 v149, v66
	s_cmp_lg_u32 s98, 0
	s_cbranch_scc1 .Led_8
	s_waitcnt vmcnt(0)
.Led_8:
	v_mov_b32_e32 v154, v66
	v_mov_b32_e32 v155, v66
	v_mov_b32_e32 v156, v66
	v_mov_b32_e32 v157, v66
	v_mov_b32_e32 v162, v66
	v_mov_b32_e32 v163, v66
	v_mov_b32_e32 v164, v66
	v_mov_b32_e32 v165, v66
	v_mov_b32_e32 v170, v66
	v_mov_b32_e32 v171, v66
	v_mov_b32_e32 v172, v66
	v_mov_b32_e32 v173, v66
	v_mov_b32_e32 v150, v66
	v_mov_b32_e32 v151, v66
	v_mov_b32_e32 v152, v66
	v_mov_b32_e32 v153, v66
	v_mov_b32_e32 v158, v66
	v_mov_b32_e32 v159, v66
	v_mov_b32_e32 v160, v66
	v_mov_b32_e32 v161, v66
	v_mov_b32_e32 v166, v66
	v_mov_b32_e32 v167, v66
	v_mov_b32_e32 v168, v66
	v_mov_b32_e32 v169, v66
	v_mov_b32_e32 v174, v66
	v_mov_b32_e32 v175, v66
	v_mov_b32_e32 v176, v66
	v_mov_b32_e32 v177, v66
	v_mov_b32_e32 v178, v66
	v_mov_b32_e32 v179, v66
	v_mov_b32_e32 v180, v66
	v_mov_b32_e32 v181, v66
	v_mov_b32_e32 v182, v66
	v_mov_b32_e32 v183, v66
	v_mov_b32_e32 v184, v66
	v_mov_b32_e32 v185, v66
	v_mov_b32_e32 v186, v66
	v_mov_b32_e32 v187, v66
	v_mov_b32_e32 v188, v66
	v_mov_b32_e32 v189, v66
	v_mov_b32_e32 v190, v66
	v_mov_b32_e32 v191, v66
	v_mov_b32_e32 v192, v66
	v_mov_b32_e32 v193, v66
	s_branch .LBB0_1868
